# same as previous with the sequential-scan phase converting items only up to 0x5400
# baseline (speedup 1.0000x reference)
.LBB0_139:
	s_cmpk_lt_i32 s97, 0x374
	s_cselect_b64 s[0:1], -1, 0
	v_writelane_b32 v253, s0, 15
	s_ashr_i32 s91, s97, 31
	s_ashr_i32 s76, s95, 31
	v_writelane_b32 v253, s1, 16
	s_lshr_b32 s0, s91, 29
	s_add_i32 s0, s97, s0
	s_ashr_i32 s3, s0, 3
	s_and_b32 s0, s0, -8
	s_sub_i32 s2, s97, s0
	s_mul_i32 s0, s2, 0x6e
	s_add_i32 s1, s0, 4
	s_cmp_eq_u32 s22, 15
	s_cselect_b64 s[4:5], -1, 0
	v_writelane_b32 v253, s4, 17
	s_cmp_eq_u32 s22, 14
	v_mov_b32_e32 v35, 0
	v_writelane_b32 v253, s5, 18
	s_cselect_b64 s[4:5], -1, 0
	v_writelane_b32 v253, s4, 19
	s_cmp_eq_u32 s22, 13
	v_mov_b32_e32 v250, 1
	v_writelane_b32 v253, s5, 20
	s_cselect_b64 s[4:5], -1, 0
	v_writelane_b32 v253, s4, 21
	s_cmp_eq_u32 s22, 12
	v_mov_b32_e32 v165, 0x358637bd
	v_writelane_b32 v253, s5, 22
	s_cselect_b64 s[4:5], -1, 0
	v_writelane_b32 v253, s4, 23
	s_cmp_eq_u32 s22, 11
	v_mov_b32_e32 v164, 0x3a27c5ac
	v_writelane_b32 v253, s5, 24
	s_cselect_b64 s[4:5], -1, 0
	v_writelane_b32 v253, s4, 25
	s_cmp_eq_u32 s22, 10
	v_mov_b32_e32 v200, 0x43e00000
	v_writelane_b32 v253, s5, 26
	s_cselect_b64 s[4:5], -1, 0
	v_writelane_b32 v253, s4, 27
	s_cmp_eq_u32 s22, 9
	v_mov_b32_e32 v202, 0x1a00
	v_writelane_b32 v253, s5, 28
	s_cselect_b64 s[4:5], -1, 0
	v_writelane_b32 v253, s4, 29
	s_cmp_eq_u32 s22, 8
	v_mov_b32_e32 v166, v35
	v_writelane_b32 v253, s5, 30
	s_cselect_b64 s[4:5], -1, 0
	v_writelane_b32 v253, s4, 31
	s_cmp_eq_u32 s22, 7
	v_mov_b32_e32 v167, v35
	v_writelane_b32 v253, s5, 32
	s_cselect_b64 s[4:5], -1, 0
	v_writelane_b32 v253, s4, 33
	s_cmp_eq_u32 s22, 6
	v_bfrev_b32_e32 v251, 0.5
	v_writelane_b32 v253, s5, 34
	s_cselect_b64 s[4:5], -1, 0
	v_writelane_b32 v253, s4, 35
	s_cmp_eq_u32 s22, 5
	v_mov_b32_e32 v201, 0x40e00000
	v_writelane_b32 v253, s5, 36
	s_cselect_b64 s[4:5], -1, 0
	v_writelane_b32 v253, s4, 37
	s_cmp_eq_u32 s22, 4
	v_mov_b32_e32 v168, 4.0
	v_writelane_b32 v253, s5, 38
	s_cselect_b64 s[4:5], -1, 0
	v_writelane_b32 v253, s4, 39
	s_cmp_eq_u32 s22, 3
	s_mov_b32 s53, 0xe000
	v_writelane_b32 v253, s5, 40
	s_cselect_b64 s[4:5], -1, 0
	v_writelane_b32 v253, s4, 41
	s_cmp_eq_u32 s22, 2
	s_movk_i32 s90, 0x1a00
	v_writelane_b32 v253, s5, 42
	s_cselect_b64 s[4:5], -1, 0
	v_writelane_b32 v253, s4, 43
	s_cmp_eq_u32 s22, 1
	s_movk_i32 s93, 0x5ff
	v_writelane_b32 v253, s5, 44
	s_cselect_b64 s[4:5], -1, 0
	v_writelane_b32 v253, s4, 45
	s_cmp_eq_u32 s22, 0
	s_mov_b32 s73, 0xfc000
	v_writelane_b32 v253, s5, 46
	s_cselect_b64 s[4:5], -1, 0
	s_lshl_b32 s0, s22, 6
	s_cmpk_lt_i32 s97, 0x440
	v_writelane_b32 v253, s4, 47
	s_cselect_b64 s[10:11], -1, 0
	s_cmpk_lt_i32 s95, 0x80
	v_writelane_b32 v253, s5, 48
	s_cselect_b64 s[12:13], -1, 0
	s_cmpk_lt_i32 s97, 0x1100
	v_writelane_b32 v253, s0, 49
	s_cselect_b64 s[4:5], -1, 0
	s_lshl_b32 s6, s97, 1
	v_writelane_b32 v253, s4, 50
	s_cmp_lt_i32 s97, 64
	s_mov_b32 s33, 0xc0e00000
	v_writelane_b32 v253, s5, 51
	s_cselect_b64 s[4:5], -1, 0
	v_writelane_b32 v253, s4, 52
	s_cmp_gt_i32 s97, 63
	s_mov_b64 s[20:21], 0x80
	v_writelane_b32 v253, s5, 53
	s_cselect_b64 s[4:5], -1, 0
	v_writelane_b32 v253, s4, 54
	s_lshl_b32 s0, s97, 9
	s_nop 0
	v_writelane_b32 v253, s5, 55
	v_writelane_b32 v253, s0, 56
	s_lshl_b32 s0, s95, 9
	v_writelane_b32 v253, s0, 57
	s_not_b32 s0, s97
	s_add_i32 s0, s95, s0
	s_lshl_b32 s0, s0, 9
	v_writelane_b32 v253, s0, 58
	s_sub_i32 s0, s97, 64
	s_sub_i32 s4, s95, 64
	s_cmpk_gt_i32 s97, 0x47f
	s_cselect_b64 s[8:9], -1, 0
	v_writelane_b32 v253, s8, 59
	s_lshl_b32 s5, s0, 3
	s_lshl_b32 s52, s4, 9
	v_writelane_b32 v253, s9, 60
	v_writelane_b32 v253, s5, 61
	s_lshl_b32 s5, s4, 3
	v_writelane_b32 v253, s5, 62
	v_writelane_b32 v253, s0, 63
	s_lshl_b32 s0, s0, 9
	v_writelane_b32 v254, s0, 0
	v_writelane_b32 v254, s4, 1
	v_writelane_b32 v254, s6, 2
	s_and_b32 s6, s6, 2
	s_or_b32 s7, s6, -15
	v_writelane_b32 v254, s7, 3
	s_or_b32 s7, s6, 0x3ffffd4
	s_ashr_i32 s4, s97, 1
	v_writelane_b32 v254, s7, 4
	s_and_b32 s5, s4, 1
	s_ashr_i32 s0, s97, 4
	v_writelane_b32 v254, s6, 5
	s_lshl_b32 s6, s6, 6
	s_cmp_eq_u32 s5, 0
	s_cselect_b64 s[8:9], -1, 0
	v_writelane_b32 v254, s8, 6
	s_lshl_b32 s7, s0, 12
	s_lshl_b32 s0, s0, 8
	v_writelane_b32 v254, s9, 7
	v_writelane_b32 v254, s7, 8
	s_addk_i32 s0, 0x4000
	v_writelane_b32 v254, s0, 9
	s_lshl_b32 s0, s97, 4
	v_writelane_b32 v254, s0, 10
	s_and_b32 s0, s0, 0xc0
	s_cmp_lt_i32 s2, 0
	s_cselect_b64 s[8:9], -1, 0
	v_writelane_b32 v254, s8, 11
	s_add_i32 s7, s95, -1
	s_cmp_lt_i32 s97, 32
	v_writelane_b32 v254, s9, 12
	v_writelane_b32 v254, s7, 13
	s_cselect_b64 s[8:9], -1, 0
	v_writelane_b32 v254, s8, 14
	s_lshl_b32 s14, s95, 4
	s_cmp_lt_i32 s2, 4
	v_writelane_b32 v254, s9, 15
	v_writelane_b32 v254, s2, 16
	s_mulk_i32 s2, 0x6f
	s_cselect_b32 s1, s2, s1
	s_add_i32 s1, s1, s3
	s_mul_hi_i32 s2, s1, 0x4ec4ec4f
	v_writelane_b32 v254, s3, 17
	s_lshr_b32 s3, s2, 31
	s_ashr_i32 s2, s2, 5
	s_add_i32 s2, s2, s3
	s_lshl_b32 s7, s2, 3
	s_mul_i32 s3, s2, 0x68
	s_sub_i32 s2, 0x44, s7
	s_min_u32 s8, s2, 8
	s_sub_i32 s1, s1, s3
	v_cvt_f32_ubyte0_e32 v2, s8
	v_cvt_f32_i32_e32 v1, s1
	v_rcp_iflag_f32_e32 v3, v2
	v_writelane_b32 v254, s10, 18
	s_ashr_i32 s2, s1, 30
	s_or_b32 s9, s2, 1
	v_writelane_b32 v254, s11, 19
	v_mul_f32_e32 v3, v1, v3
	v_writelane_b32 v254, s12, 20
	v_trunc_f32_e32 v3, v3
	s_and_b64 s[2:3], s[12:13], s[10:11]
	v_writelane_b32 v254, s13, 21
	v_fma_f32 v1, -v3, v2, v1
	v_writelane_b32 v254, s2, 22
	s_mul_i32 s10, s5, 0x4400
	s_mov_b32 s13, 0xc3e00000
	v_writelane_b32 v254, s3, 23
	v_cmp_ge_f32_e64 s[2:3], |v1|, v2
	v_cvt_i32_f32_e32 v1, v3
	s_and_b64 s[2:3], s[2:3], exec
	s_cselect_b32 s2, s9, 0
	s_mov_b32 s12, 0x3b800000
	v_readfirstlane_b32 s3, v1
	s_add_i32 s2, s3, s2
	s_mul_i32 s3, s2, s8
	s_abs_i32 s8, s95
	v_cvt_f32_u32_e32 v1, s8
	s_sub_i32 s1, s1, s3
	s_sext_i32_i8 s1, s1
	s_add_i32 s7, s7, s1
	v_rcp_iflag_f32_e32 v1, v1
	s_sub_i32 s1, 0, s8
	v_mul_f32_e32 v1, 0x4f7ffffe, v1
	v_cvt_u32_f32_e32 v1, v1
	s_nop 0
	v_readfirstlane_b32 s3, v1
	s_mul_i32 s1, s1, s3
	s_mul_hi_u32 s1, s3, s1
	s_add_i32 s9, s3, s1
	s_sext_i32_i8 s1, s2
	s_bfe_i64 s[2:3], s[2:3], 0x80000
	v_writelane_b32 v254, s1, 24
	s_lshl_b64 s[2:3], s[2:3], 19
	v_writelane_b32 v254, s2, 25
	s_mul_hi_u32 s1, s9, 0x374
	s_mul_i32 s1, s1, s8
	v_writelane_b32 v254, s3, 26
	v_writelane_b32 v254, s7, 27
	s_lshl_b32 s2, s7, 8
	s_sub_i32 s1, 0x374, s1
	v_writelane_b32 v254, s2, 28
	s_bitset1_b32 s2, 7
	v_writelane_b32 v254, s2, 29
	s_sub_i32 s2, s1, s8
	s_cmp_ge_u32 s1, s8
	s_cselect_b32 s1, s2, s1
	s_sub_i32 s2, s1, s8
	s_cmp_ge_u32 s1, s8
	s_cselect_b32 s1, s2, s1
	s_cmp_ge_i32 s97, s1
	s_cselect_b64 s[2:3], -1, 0
	v_writelane_b32 v254, s2, 30
	v_mbcnt_lo_u32_b32 v1, -1, 0
	v_mbcnt_hi_u32_b32 v203, -1, v1
	v_writelane_b32 v254, s3, 31
	s_sub_i32 s2, s97, s1
	s_sub_i32 s1, s95, s1
	s_lshl_b32 s49, s1, 3
	s_mul_hi_u32 s1, s9, 0x110
	s_mul_i32 s1, s1, s8
	s_lshl_b32 s2, s2, 3
	s_sub_i32 s1, 0x110, s1
	v_writelane_b32 v254, s2, 32
	s_sub_i32 s2, s1, s8
	s_cmp_ge_u32 s1, s8
	s_cselect_b32 s1, s2, s1
	v_writelane_b32 v254, s9, 33
	s_sub_i32 s2, s1, s8
	v_writelane_b32 v254, s8, 34
	s_cmp_ge_u32 s1, s8
	s_mov_b32 s8, 0
	s_cselect_b32 s1, s2, s1
	s_mov_b32 s9, 1
	s_mov_b32 s11, s8
	v_writelane_b32 v254, s10, 35
	s_cmp_ge_i32 s97, s1
	s_mul_hi_i32 s3, s4, 0x61c000
	v_writelane_b32 v254, s11, 36
	s_cselect_b64 s[10:11], -1, 0
	v_writelane_b32 v254, s10, 37
	s_sub_i32 s2, s97, s1
	s_sub_i32 s1, s95, s1
	v_writelane_b32 v254, s11, 38
	s_lshl_b32 s2, s2, 3
	s_lshl_b32 s1, s1, 3
	v_writelane_b32 v254, s1, 39
	s_add_i32 s1, s2, 0x5400
	v_writelane_b32 v254, s1, 40
	s_lshl_b32 s1, s95, 1
	v_writelane_b32 v254, s1, 41
	s_lshl_b32 s1, s97, 11
	v_writelane_b32 v254, s1, 42
	s_lshl_b32 s1, s95, 11
	s_mul_i32 s4, s4, 0x61c000
	v_writelane_b32 v254, s1, 43
	s_add_i32 s1, s1, 0xfffe0000
	v_writelane_b32 v254, s1, 44
	s_add_u32 s1, s4, 0x796f4000
	v_writelane_b32 v254, s1, 45
	s_addc_u32 s1, s3, 0
	v_writelane_b32 v254, s1, 46
	s_or_b32 s1, s6, 0xffffef00
	v_writelane_b32 v254, s1, 47
	s_add_u32 s1, s4, 0x796f3000
	v_writelane_b32 v254, s1, 48
	s_addc_u32 s1, s3, 0
	v_writelane_b32 v254, s1, 49
	s_or_b32 s1, s6, 64
	v_writelane_b32 v254, s1, 50
	s_add_u32 s1, s4, 0x79710c00
	v_writelane_b32 v254, s1, 51
	s_addc_u32 s1, s3, 0
	v_writelane_b32 v254, s1, 52
	v_writelane_b32 v254, s4, 53
	s_add_u32 s1, s4, 0x7970fc00
	v_writelane_b32 v254, s1, 54
	v_writelane_b32 v254, s3, 55
	s_addc_u32 s1, s3, 0
	v_writelane_b32 v254, s1, 56
	s_lshl_b32 s1, s95, 6
	v_writelane_b32 v254, s1, 57
	s_add_u32 s1, s82, 0x1000
	v_writelane_b32 v254, s1, 58
	s_addc_u32 s1, s83, 0
	v_writelane_b32 v254, s1, 59
	s_lshl_b32 s0, s0, 1
	v_writelane_b32 v254, s0, 60
	s_add_i32 s0, 0, 0x20800
	v_writelane_b32 v254, s0, 61
	s_add_i32 s0, 0, 0x20804
	v_writelane_b32 v254, s0, 62
	s_add_i32 s0, 0, 0xfc0
	v_writelane_b32 v254, s0, 63
	s_add_i32 s0, 0, 0x8c00
	v_writelane_b32 v255, s0, 0
	s_add_i32 s0, 0, 0x10100
	v_writelane_b32 v255, s0, 1
	s_add_i32 s0, 0, 0x208bc
	v_writelane_b32 v255, s0, 2
	s_add_i32 s0, 0, 0x209bc
	v_writelane_b32 v255, s0, 3
	s_add_i32 s0, 0, 0x20844
	v_writelane_b32 v255, s0, 4
	s_add_i32 s0, 0, 0x2084c
	v_writelane_b32 v255, s0, 5
	s_add_i32 s0, 0, 0x20854
	v_writelane_b32 v255, s0, 6
	s_add_i32 s0, 0, 0x2085c
	v_writelane_b32 v255, s0, 7
	s_add_i32 s0, 0, 0x20864
	v_writelane_b32 v255, s0, 8
	s_add_i32 s0, 0, 0x2086c
	v_writelane_b32 v255, s0, 9
	s_add_i32 s0, 0, 0x20874
	v_writelane_b32 v255, s0, 10
	s_add_i32 s0, 0, 0x2087c
	v_writelane_b32 v255, s0, 11
	s_add_i32 s0, 0, 0x20884
	v_writelane_b32 v255, s0, 12
	s_add_i32 s0, 0, 0x2088c
	v_writelane_b32 v255, s0, 13
	s_add_i32 s0, 0, 0x20894
	v_writelane_b32 v255, s0, 14
	s_add_i32 s0, 0, 0x2089c
	v_writelane_b32 v255, s0, 15
	s_add_i32 s0, 0, 0x208a4
	v_writelane_b32 v255, s0, 16
	s_add_i32 s0, 0, 0x208ac
	s_ashr_i32 s15, s14, 31
	v_writelane_b32 v255, s0, 17
	s_add_i32 s0, 0, 0x208b4
	v_writelane_b32 v255, s0, 18
	s_lshl_b64 s[0:1], s[14:15], 12
	v_writelane_b32 v255, s0, 19
	s_nop 1
	v_writelane_b32 v255, s1, 20
	s_lshl_b64 s[0:1], s[14:15], 11
	v_writelane_b32 v255, s0, 21
	s_nop 1
	v_writelane_b32 v255, s1, 22
	s_lshl_b64 s[0:1], s[14:15], 4
	v_writelane_b32 v255, s0, 23
	s_nop 1
	v_writelane_b32 v255, s1, 24
	s_mov_b64 s[0:1], 0x10000
	v_writelane_b32 v255, s0, 25
	s_nop 1
	v_writelane_b32 v255, s1, 26
	v_writelane_b32 v255, s95, 27
	v_writelane_b32 v255, s28, 28
	s_mov_b32 s0, s14
	s_nop 0
	v_writelane_b32 v255, s29, 29
	v_writelane_b32 v255, s91, 30
	v_writelane_b32 v255, s76, 31
	v_writelane_b32 v255, s52, 32
	v_writelane_b32 v255, s0, 33
	s_nop 1
	v_writelane_b32 v255, s1, 34
	v_writelane_b32 v255, s49, 35
	v_writelane_b32 v255, s97, 36
	s_branch .LBB0_142

.LBB0_624:
	v_readlane_b32 s0, v255, 57
	s_movk_i32 s92, 0x2000
	v_readlane_b32 s1, v255, 58
	s_or_b64 exec, exec, s[0:1]
	v_readlane_b32 s0, v255, 50
	v_readlane_b32 s1, v255, 51
	s_and_b64 s[0:1], s[0:1], exec
	s_mov_b32 s0, 0xc000
	s_cselect_b32 s30, s0, 0x5400
	v_readlane_b32 s0, v253, 14
	v_readlane_b32 s4, v255, 52
	s_add_i32 s29, s4, s0
	s_lshl_b32 s0, s4, 14
	v_readlane_b32 s80, v255, 40
	s_add_i32 s28, s0, 0
	s_add_i32 s31, s29, 0x3400
	v_readlane_b32 s81, v255, 41
	v_readlane_b32 s84, v255, 44
	v_readlane_b32 s85, v255, 45
	v_readlane_b32 s86, v255, 46
	v_readlane_b32 s87, v255, 47
	s_cmp_ge_i32 s31, s30
	v_readlane_b32 s82, v255, 42
	v_readlane_b32 s83, v255, 43
	s_waitcnt vmcnt(0) lgkmcnt(0)
	s_barrier
	s_cbranch_scc1 .LBB0_644
	s_mul_hi_i32 s0, s31, 0x2aaaaaab
	s_lshr_b32 s1, s0, 31
	s_ashr_i32 s0, s0, 8
	s_add_i32 s0, s0, s1
	s_mul_i32 s1, s0, 0x600
	s_sub_i32 s3, s31, s1
	s_cmpk_gt_i32 s3, 0x3ff
	s_mov_b64 s[8:9], -1
	s_cbranch_scc0 .LBB0_627
	v_readlane_b32 s4, v255, 37
	s_ashr_i32 s1, s0, 31
	v_readlane_b32 s5, v255, 38
	v_readlane_b32 s36, v252, 48
	s_lshl_b32 s2, s4, 27
	s_lshl_b64 s[4:5], s[0:1], 22
	v_readlane_b32 s40, v252, 52
	v_readlane_b32 s41, v252, 53
	s_add_u32 s1, s40, s4
	s_addc_u32 s5, s41, s5
	s_add_u32 s4, s1, s2
	s_addc_u32 s5, s5, 0
	s_lshl_b32 s1, s3, 1
	s_and_b32 s1, s1, 0x7fffffc0
	s_lshl_b32 s2, s3, 5
	v_readlane_b32 s37, v252, 49
	v_readlane_b32 s38, v252, 50
	v_readlane_b32 s39, v252, 51
	v_readlane_b32 s42, v252, 54
	v_readlane_b32 s43, v252, 55
	s_addk_i32 s1, 0xf800
	s_and_b32 s2, s2, 0x3e0
	s_mov_b64 s[8:9], 0

.LBB0_770:
	s_or_b64 exec, exec, s[0:1]
	v_readlane_b32 s0, v255, 50
	v_readlane_b32 s1, v255, 51
	s_and_b64 s[0:1], s[0:1], exec
	s_mov_b32 s0, 0xc000
	s_cselect_b32 s34, s0, 0x5400
	v_readlane_b32 s0, v253, 61
	v_readlane_b32 s1, v255, 52
	s_add_i32 s31, s1, s0
	s_lshl_b32 s0, s1, 14
	s_add_i32 s30, s0, 0
	s_add_i32 s35, s31, 0x3400
	s_cmp_ge_i32 s35, s34
	s_cbranch_scc1 .LBB0_789
	s_mul_hi_i32 s0, s35, 0x2aaaaaab
	s_lshr_b32 s1, s0, 31
	s_ashr_i32 s0, s0, 8
	s_add_i32 s0, s0, s1
	s_mul_i32 s1, s0, 0x600
	s_sub_i32 s5, s35, s1
	s_cmpk_gt_i32 s5, 0x3ff
	s_mov_b64 s[10:11], -1
	s_cbranch_scc0 .LBB0_773
	s_ashr_i32 s1, s0, 31
	v_readlane_b32 s6, v255, 37
	v_readlane_b32 s36, v252, 48
	s_lshl_b32 s4, s6, 27
	s_lshl_b64 s[8:9], s[0:1], 22
	v_readlane_b32 s40, v252, 52
	v_readlane_b32 s41, v252, 53
	s_add_u32 s1, s40, s8
	s_addc_u32 s9, s41, s9
	s_add_u32 s8, s1, s4
	s_addc_u32 s9, s9, 0
	s_lshl_b32 s1, s5, 1
	s_and_b32 s1, s1, 0x7fffffc0
	s_lshl_b32 s4, s5, 5
	v_readlane_b32 s7, v255, 38
	v_readlane_b32 s37, v252, 49
	v_readlane_b32 s38, v252, 50
	v_readlane_b32 s39, v252, 51
	v_readlane_b32 s42, v252, 54
	v_readlane_b32 s43, v252, 55
	s_addk_i32 s1, 0xf800
	s_and_b32 s4, s4, 0x3e0
	s_mov_b64 s[10:11], 0
